# bn_kernel: BN-stat loads issued before the streaming row loads so the coefficient math overlaps the stream
# speedup vs baseline: 1.0300x; 1.0178x over previous
.LBB2_4:
	s_lshr_b32 s2, s2, 3
	s_add_i32 s2, s10, s2
	v_lshrrev_b32_e32 v2, 4, v0
	s_load_dwordx4 s[4:7], s[0:1], 0x8
	s_load_dwordx4 s[16:19], s[0:1], 0x18
	s_load_dwordx2 s[20:21], s[0:1], 0x28
	v_lshl_or_b32 v58, s2, 6, v2
	v_min_i32_e32 v2, 0x1869f, v58
	v_and_b32_e32 v1, 15, v0
	v_ashrrev_i32_e32 v3, 31, v2
	v_lshlrev_b64 v[2:3], 8, v[2:3]
	v_lshlrev_b32_e32 v50, 4, v1
	v_or_b32_e32 v2, v2, v50
	s_waitcnt lgkmcnt(0)
	s_movk_i32 s2, 0x80
	v_cmp_gt_u32_e32 vcc, s2, v0
	s_mov_b64 s[22:23], vcc
	v_mov_b32_e32 v35, 0
	s_and_saveexec_b64 s[2:3], vcc
	s_cbranch_execz .Lbn_stats_issued
	v_lshlrev_b32_e32 v34, 2, v0
	v_and_b32_e32 v51, 7, v0
	v_lshrrev_b32_e32 v0, 1, v0
	global_load_dword v37, v34, s[16:17]
	global_load_dword v36, v34, s[16:17] offset:512
	global_load_dword v39, v34, s[16:17] offset:1024
	global_load_dword v38, v34, s[16:17] offset:1536
	global_load_dword v41, v34, s[16:17] offset:2048
	global_load_dword v40, v34, s[16:17] offset:2560
	global_load_dword v43, v34, s[16:17] offset:3072
	global_load_dword v42, v34, s[16:17] offset:3584
	v_lshl_add_u64 v[44:45], s[16:17], 0, v[34:35]
	v_add_co_u32_e32 v62, vcc, 0x1000, v44
	v_and_b32_e32 v0, 60, v0
	s_nop 0
	v_addc_co_u32_e32 v63, vcc, 0, v45, vcc
	global_load_dword v45, v[62:63], off
	global_load_dword v44, v[62:63], off offset:512
	global_load_dword v47, v[62:63], off offset:1024
	global_load_dword v46, v[62:63], off offset:1536
	global_load_dword v49, v[62:63], off offset:2048
	global_load_dword v48, v[62:63], off offset:2560
	global_load_dword v61, v[62:63], off offset:3072
	global_load_dword v60, v[62:63], off offset:3584
	v_or_b32_e32 v52, v0, v51
	v_add3_u32 v0, v51, v0, 60
	v_cmp_gt_u32_e32 vcc, 4, v51
	s_nop 1
	v_cndmask_b32_e32 v0, v0, v52, vcc
	v_lshlrev_b32_e32 v0, 2, v0
	global_load_dword v51, v0, s[18:19]
	s_nop 0
	global_load_dword v0, v0, s[20:21]
.Lbn_stats_issued:
	s_or_b64 exec, exec, s[2:3]
	v_lshl_add_u64 v[4:5], s[8:9], 0, v[2:3]
	v_lshl_add_u64 v[2:3], s[4:5], 0, v[2:3]
	v_or_b32_e32 v56, 16, v58
	global_load_dwordx4 v[30:33], v[2:3], off nt
	v_min_i32_e32 v2, 0x1869f, v56
	v_ashrrev_i32_e32 v3, 31, v2
	v_lshlrev_b64 v[2:3], 8, v[2:3]
	v_or_b32_e32 v2, v2, v50
	global_load_dwordx4 v[26:29], v[4:5], off
	v_lshl_add_u64 v[4:5], s[8:9], 0, v[2:3]
	v_lshl_add_u64 v[2:3], s[4:5], 0, v[2:3]
	v_or_b32_e32 v54, 32, v58
	global_load_dwordx4 v[22:25], v[2:3], off nt
	v_min_i32_e32 v2, 0x1869f, v54
	v_ashrrev_i32_e32 v3, 31, v2
	v_lshlrev_b64 v[2:3], 8, v[2:3]
	v_or_b32_e32 v2, v2, v50
	global_load_dwordx4 v[18:21], v[4:5], off
	v_lshl_add_u64 v[4:5], s[8:9], 0, v[2:3]
	v_lshl_add_u64 v[2:3], s[4:5], 0, v[2:3]
	v_or_b32_e32 v59, 48, v58
	global_load_dwordx4 v[14:17], v[2:3], off nt
	v_min_i32_e32 v2, 0x1869f, v59
	v_ashrrev_i32_e32 v3, 31, v2
	v_lshlrev_b64 v[6:7], 8, v[2:3]
	v_or_b32_e32 v6, v6, v50
	v_lshl_add_u64 v[2:3], s[8:9], 0, v[6:7]
	v_lshl_add_u64 v[6:7], s[4:5], 0, v[6:7]
	global_load_dwordx4 v[10:13], v[4:5], off
	global_load_dwordx4 v[2:5], v[2:3], off
	v_mov_b32_e32 v35, 0
	global_load_dwordx4 v[6:9], v[6:7], off nt
	s_and_saveexec_b64 s[2:3], s[22:23]
	s_cbranch_execz .LBB2_6
	s_mov_b32 s8, 0
	s_mov_b32 s9, 0x40f86a00
	s_brev_b32 s4, 1
	s_mov_b32 s5, 0x3ee4f8b5
	s_mov_b32 s12, 0
	s_brev_b32 s13, 8
	v_mov_b32_e32 v35, 0x100
	s_waitcnt vmcnt(24)
	v_pk_add_f32 v[36:37], v[36:37], 0 op_sel_hi:[1,0]
	s_waitcnt vmcnt(22)
	v_pk_add_f32 v[36:37], v[36:37], v[38:39]
	s_waitcnt vmcnt(20)
	v_pk_add_f32 v[36:37], v[36:37], v[40:41]
	s_waitcnt vmcnt(18)
	v_pk_add_f32 v[36:37], v[36:37], v[42:43]
	s_waitcnt vmcnt(16)
	v_pk_add_f32 v[36:37], v[36:37], v[44:45]
	s_waitcnt vmcnt(14)
	v_pk_add_f32 v[36:37], v[36:37], v[46:47]
	s_waitcnt vmcnt(12)
	v_pk_add_f32 v[36:37], v[36:37], v[48:49]
	s_waitcnt vmcnt(10)
	v_pk_add_f32 v[36:37], v[36:37], v[60:61]
	s_nop 0
	v_cvt_f64_f32_e32 v[38:39], v37
	v_cvt_f64_f32_e32 v[36:37], v36
	v_div_scale_f64 v[40:41], s[0:1], s[8:9], s[8:9], v[36:37]
	v_div_scale_f64 v[44:45], s[0:1], s[8:9], s[8:9], v[38:39]
	v_rcp_f64_e32 v[46:47], v[40:41]
	v_rcp_f64_e32 v[48:49], v[44:45]
	v_div_scale_f64 v[42:43], vcc, v[36:37], s[8:9], v[36:37]
	v_fma_f64 v[62:63], -v[40:41], v[46:47], 1.0
	v_fma_f64 v[52:53], -v[44:45], v[48:49], 1.0
	v_fmac_f64_e32 v[46:47], v[46:47], v[62:63]
	v_fmac_f64_e32 v[48:49], v[48:49], v[52:53]
	v_fma_f64 v[52:53], -v[40:41], v[46:47], 1.0
	v_fma_f64 v[62:63], -v[44:45], v[48:49], 1.0
	v_fmac_f64_e32 v[46:47], v[46:47], v[52:53]
	v_div_scale_f64 v[60:61], s[0:1], v[38:39], s[8:9], v[38:39]
	v_fmac_f64_e32 v[48:49], v[48:49], v[62:63]
	v_mul_f64 v[52:53], v[42:43], v[46:47]
	v_mul_f64 v[62:63], v[60:61], v[48:49]
	v_fma_f64 v[40:41], -v[40:41], v[52:53], v[42:43]
	v_fma_f64 v[42:43], -v[44:45], v[62:63], v[60:61]
	v_div_fmas_f64 v[40:41], v[40:41], v[46:47], v[52:53]
	s_mov_b64 vcc, s[0:1]
	v_div_fixup_f64 v[36:37], v[40:41], s[8:9], v[36:37]
	v_div_fmas_f64 v[40:41], v[42:43], v[48:49], v[62:63]
	v_div_fixup_f64 v[38:39], v[40:41], s[8:9], v[38:39]
	v_fma_f64 v[36:37], -v[38:39], v[38:39], v[36:37]
	v_cmp_ngt_f64_e32 vcc, 0, v[36:37]
	v_mov_b32_e32 v46, 0x260
	v_or_b32_e32 v60, 48, v58
	v_cndmask_b32_e32 v37, 0, v37, vcc
	v_cndmask_b32_e32 v36, 0, v36, vcc
	v_add_f64 v[36:37], v[36:37], s[4:5]
	v_cmp_gt_f64_e32 vcc, s[12:13], v[36:37]
	s_nop 1
	v_cndmask_b32_e32 v35, 0, v35, vcc
	v_ldexp_f64 v[36:37], v[36:37], v35
	v_rsq_f64_e32 v[40:41], v[36:37]
	v_mov_b32_e32 v35, 0xffffff80
	v_cndmask_b32_e32 v35, 0, v35, vcc
	v_cmp_class_f64_e32 vcc, v[36:37], v46
	v_mul_f64 v[42:43], v[36:37], v[40:41]
	v_mul_f64 v[40:41], v[40:41], 0.5
	v_fma_f64 v[44:45], -v[40:41], v[42:43], 0.5
	v_fmac_f64_e32 v[42:43], v[42:43], v[44:45]
	v_fmac_f64_e32 v[40:41], v[40:41], v[44:45]
	v_fma_f64 v[44:45], -v[42:43], v[42:43], v[36:37]
	v_fmac_f64_e32 v[42:43], v[44:45], v[40:41]
	v_fma_f64 v[44:45], -v[42:43], v[42:43], v[36:37]
	v_fmac_f64_e32 v[42:43], v[44:45], v[40:41]
	v_ldexp_f64 v[40:41], v[42:43], v35
	v_cndmask_b32_e32 v37, v41, v37, vcc
	v_cndmask_b32_e32 v36, v40, v36, vcc
	v_div_scale_f64 v[40:41], s[0:1], v[36:37], v[36:37], 1.0
	v_rcp_f64_e32 v[42:43], v[40:41]
	v_div_scale_f64 v[44:45], vcc, 1.0, v[36:37], 1.0
	v_fma_f64 v[46:47], -v[40:41], v[42:43], 1.0
	v_fmac_f64_e32 v[42:43], v[42:43], v[46:47]
	v_fma_f64 v[46:47], -v[40:41], v[42:43], 1.0
	v_fmac_f64_e32 v[42:43], v[42:43], v[46:47]
	v_mul_f64 v[46:47], v[44:45], v[42:43]
	v_fma_f64 v[40:41], -v[40:41], v[46:47], v[44:45]
	v_div_fmas_f64 v[40:41], v[40:41], v[42:43], v[46:47]
	v_div_fixup_f64 v[36:37], v[40:41], v[36:37], 1.0
	v_cvt_f32_f64_e32 v35, v[36:37]
	s_waitcnt vmcnt(9)
	v_mul_f32_e32 v35, v51, v35
	v_cvt_f32_f64_e32 v36, v[38:39]
	s_waitcnt vmcnt(8)
	v_fma_f32 v0, -v35, v36, v0
	ds_write2st64_b32 v34, v35, v0 offset1:2
.LBB2_6:
	s_or_b64 exec, exec, s[2:3]
	v_or_b32_e32 v60, 48, v58
	v_lshlrev_b32_e32 v0, 5, v1
	s_waitcnt lgkmcnt(0)
	s_barrier
	ds_read_b128 v[42:45], v0
	ds_read_b128 v[34:37], v0 offset:16
	ds_read_b128 v[46:49], v0 offset:512
	ds_read_b128 v[38:41], v0 offset:528
	s_mov_b32 s2, 0x186a0
	v_cmp_gt_i32_e32 vcc, s2, v58
	s_and_saveexec_b64 s[0:1], vcc
	s_cbranch_execnz .LBB2_11
	s_or_b64 exec, exec, s[0:1]
	v_cmp_gt_i32_e32 vcc, s2, v56
	s_and_saveexec_b64 s[0:1], vcc
	s_cbranch_execnz .LBB2_12

	.amdhsa_kernel _Z9bn_kernelPKDv8_DF16_S1_PS_PKfS4_S4_
		.amdhsa_group_segment_fixed_size 1024
		.amdhsa_private_segment_fixed_size 0
		.amdhsa_kernarg_size 304
		.amdhsa_user_sgpr_count 2
		.amdhsa_user_sgpr_dispatch_ptr 0
		.amdhsa_user_sgpr_queue_ptr 0
		.amdhsa_user_sgpr_kernarg_segment_ptr 1
		.amdhsa_user_sgpr_dispatch_id 0
		.amdhsa_user_sgpr_kernarg_preload_length 0
		.amdhsa_user_sgpr_kernarg_preload_offset 0
		.amdhsa_user_sgpr_private_segment_size 0
		.amdhsa_uses_dynamic_stack 0
		.amdhsa_enable_private_segment 0
		.amdhsa_system_sgpr_workgroup_id_x 1
		.amdhsa_system_sgpr_workgroup_id_y 0
		.amdhsa_system_sgpr_workgroup_id_z 0
		.amdhsa_system_sgpr_workgroup_info 0
		.amdhsa_system_vgpr_workitem_id 0
		.amdhsa_next_free_vgpr 64
		.amdhsa_next_free_sgpr 24
		.amdhsa_accum_offset 64
		.amdhsa_reserve_vcc 1
		.amdhsa_float_round_mode_32 0
		.amdhsa_float_round_mode_16_64 0
		.amdhsa_float_denorm_mode_32 3
		.amdhsa_float_denorm_mode_16_64 3
		.amdhsa_dx10_clamp 1
		.amdhsa_ieee_mode 1
		.amdhsa_fp16_overflow 0
		.amdhsa_tg_split 0
		.amdhsa_exception_fp_ieee_invalid_op 0
		.amdhsa_exception_fp_denorm_src 0
		.amdhsa_exception_fp_ieee_div_zero 0
		.amdhsa_exception_fp_ieee_overflow 0
		.amdhsa_exception_fp_ieee_underflow 0
		.amdhsa_exception_fp_ieee_inexact 0
		.amdhsa_exception_int_div_zero 0
	.end_amdhsa_kernel

amdhsa.kernels:
  - .agpr_count:     0
    .args:
      - .actual_access:  read_only
        .address_space:  global
        .offset:         0
        .size:           8
        .value_kind:     global_buffer
      - .address_space:  global
        .offset:         8
        .size:           8
        .value_kind:     global_buffer
      - .actual_access:  read_only
        .address_space:  global
        .offset:         16
        .size:           8
        .value_kind:     global_buffer
      - .actual_access:  read_only
        .address_space:  global
        .offset:         24
        .size:           8
        .value_kind:     global_buffer
      - .actual_access:  write_only
        .address_space:  global
        .offset:         32
        .size:           8
        .value_kind:     global_buffer
      - .actual_access:  read_only
        .address_space:  global
        .offset:         40
        .size:           8
        .value_kind:     global_buffer
      - .actual_access:  write_only
        .address_space:  global
        .offset:         48
        .size:           8
        .value_kind:     global_buffer
      - .actual_access:  write_only
        .address_space:  global
        .offset:         56
        .size:           8
        .value_kind:     global_buffer
    .group_segment_fixed_size: 6400
    .kernarg_segment_align: 8
    .kernarg_segment_size: 64
    .language:       OpenCL C
    .language_version:
      - 2
      - 0
    .max_flat_workgroup_size: 1024
    .name:           _Z17prep_count_kernelPKfPDv8_DF16_S0_S0_S2_PKiPiP15HIP_vector_typeIfLj4EE
    .private_segment_fixed_size: 0
    .sgpr_count:     22
    .sgpr_spill_count: 0
    .symbol:         _Z17prep_count_kernelPKfPDv8_DF16_S0_S0_S2_PKiPiP15HIP_vector_typeIfLj4EE.kd
    .uniform_work_group_size: 1
    .uses_dynamic_stack: false
    .vgpr_count:     22
    .vgpr_spill_count: 0
    .wavefront_size: 64
  - .agpr_count:     0
    .args:
      - .actual_access:  read_only
        .address_space:  global
        .offset:         0
        .size:           8
        .value_kind:     global_buffer
      - .actual_access:  read_only
        .address_space:  global
        .offset:         8
        .size:           8
        .value_kind:     global_buffer
      - .actual_access:  read_only
        .address_space:  global
        .offset:         16
        .size:           8
        .value_kind:     global_buffer
      - .actual_access:  write_only
        .address_space:  global
        .offset:         24
        .size:           8
        .value_kind:     global_buffer
      - .actual_access:  write_only
        .address_space:  global
        .offset:         32
        .size:           8
        .value_kind:     global_buffer
    .group_segment_fixed_size: 124704
    .kernarg_segment_align: 8
    .kernarg_segment_size: 40
    .language:       OpenCL C
    .language_version:
      - 2
      - 0
    .max_flat_workgroup_size: 1024
    .name:           _Z14scatter_kernelPKiS0_S0_PiP15HIP_vector_typeIiLj2EE
    .private_segment_fixed_size: 0
    .sgpr_count:     55
    .sgpr_spill_count: 0
    .symbol:         _Z14scatter_kernelPKiS0_S0_PiP15HIP_vector_typeIiLj2EE.kd
    .uniform_work_group_size: 1
    .uses_dynamic_stack: false
    .vgpr_count:     100
    .vgpr_spill_count: 0
    .wavefront_size: 64
  - .agpr_count:     0
    .args:
      - .actual_access:  read_only
        .address_space:  global
        .offset:         0
        .size:           8
        .value_kind:     global_buffer
      - .address_space:  global
        .offset:         8
        .size:           8
        .value_kind:     global_buffer
      - .address_space:  global
        .offset:         16
        .size:           8
        .value_kind:     global_buffer
      - .actual_access:  read_only
        .address_space:  global
        .offset:         24
        .size:           8
        .value_kind:     global_buffer
      - .actual_access:  read_only
        .address_space:  global
        .offset:         32
        .size:           8
        .value_kind:     global_buffer
      - .actual_access:  read_only
        .address_space:  global
        .offset:         40
        .size:           8
        .value_kind:     global_buffer
      - .offset:         48
        .size:           4
        .value_kind:     hidden_block_count_x
      - .offset:         52
        .size:           4
        .value_kind:     hidden_block_count_y
      - .offset:         56
        .size:           4
        .value_kind:     hidden_block_count_z
      - .offset:         60
        .size:           2
        .value_kind:     hidden_group_size_x
      - .offset:         62
        .size:           2
        .value_kind:     hidden_group_size_y
      - .offset:         64
        .size:           2
        .value_kind:     hidden_group_size_z
      - .offset:         66
        .size:           2
        .value_kind:     hidden_remainder_x
      - .offset:         68
        .size:           2
        .value_kind:     hidden_remainder_y
      - .offset:         70
        .size:           2
        .value_kind:     hidden_remainder_z
      - .offset:         88
        .size:           8
        .value_kind:     hidden_global_offset_x
      - .offset:         96
        .size:           8
        .value_kind:     hidden_global_offset_y
      - .offset:         104
        .size:           8
        .value_kind:     hidden_global_offset_z
      - .offset:         112
        .size:           2
        .value_kind:     hidden_grid_dims
    .group_segment_fixed_size: 1024
    .kernarg_segment_align: 8
    .kernarg_segment_size: 304
    .language:       OpenCL C
    .language_version:
      - 2
      - 0
    .max_flat_workgroup_size: 256
    .name:           _Z9bn_kernelPKDv8_DF16_S1_PS_PKfS4_S4_
    .private_segment_fixed_size: 0
    .sgpr_count:     30
    .sgpr_spill_count: 0
    .symbol:         _Z9bn_kernelPKDv8_DF16_S1_PS_PKfS4_S4_.kd
    .uniform_work_group_size: 1
    .uses_dynamic_stack: false
    .vgpr_count:     64
    .vgpr_spill_count: 0
    .wavefront_size: 64
  - .agpr_count:     0
    .args:
      - .actual_access:  read_only
        .address_space:  global
        .offset:         0
        .size:           8
        .value_kind:     global_buffer
      - .actual_access:  read_only
        .address_space:  global
        .offset:         8
        .size:           8
        .value_kind:     global_buffer
      - .actual_access:  read_only
        .address_space:  global
        .offset:         16
        .size:           8
        .value_kind:     global_buffer
      - .actual_access:  read_only
        .address_space:  global
        .offset:         24
        .size:           8
        .value_kind:     global_buffer
      - .actual_access:  read_only
        .address_space:  global
        .offset:         32
        .size:           8
        .value_kind:     global_buffer
      - .actual_access:  read_only
        .address_space:  global
        .offset:         40
        .size:           8
        .value_kind:     global_buffer
      - .actual_access:  read_only
        .address_space:  global
        .offset:         48
        .size:           8
        .value_kind:     global_buffer
      - .actual_access:  write_only
        .address_space:  global
        .offset:         56
        .size:           8
        .value_kind:     global_buffer
      - .offset:         64
        .size:           4
        .value_kind:     hidden_block_count_x
      - .offset:         68
        .size:           4
        .value_kind:     hidden_block_count_y
      - .offset:         72
        .size:           4
        .value_kind:     hidden_block_count_z
      - .offset:         76
        .size:           2
        .value_kind:     hidden_group_size_x
      - .offset:         78
        .size:           2
        .value_kind:     hidden_group_size_y
      - .offset:         80
        .size:           2
        .value_kind:     hidden_group_size_z
      - .offset:         82
        .size:           2
        .value_kind:     hidden_remainder_x
      - .offset:         84
        .size:           2
        .value_kind:     hidden_remainder_y
      - .offset:         86
        .size:           2
        .value_kind:     hidden_remainder_z
      - .offset:         104
        .size:           8
        .value_kind:     hidden_global_offset_x
      - .offset:         112
        .size:           8
        .value_kind:     hidden_global_offset_y
      - .offset:         120
        .size:           8
        .value_kind:     hidden_global_offset_z
      - .offset:         128
        .size:           2
        .value_kind:     hidden_grid_dims
    .group_segment_fixed_size: 34816
    .kernarg_segment_align: 8
    .kernarg_segment_size: 320
    .language:       OpenCL C
    .language_version:
      - 2
      - 0
    .max_flat_workgroup_size: 512
    .name:           _Z12final_kernelPKDv8_DF16_S1_PKfS3_S3_S1_S3_Pf
    .private_segment_fixed_size: 0
    .sgpr_count:     28
    .sgpr_spill_count: 0
    .symbol:         _Z12final_kernelPKDv8_DF16_S1_PKfS3_S3_S1_S3_Pf.kd
    .uniform_work_group_size: 1
    .uses_dynamic_stack: false
    .vgpr_count:     60
    .vgpr_spill_count: 0
    .wavefront_size: 64
  - .agpr_count:     0
    .args:
      - .actual_access:  read_only
        .address_space:  global
        .offset:         0
        .size:           8
        .value_kind:     global_buffer
      - .actual_access:  read_only
        .address_space:  global
        .offset:         8
        .size:           8
        .value_kind:     global_buffer
      - .address_space:  global
        .offset:         16
        .size:           8
        .value_kind:     global_buffer
      - .actual_access:  write_only
        .address_space:  global
        .offset:         24
        .size:           8
        .value_kind:     global_buffer
      - .address_space:  global
        .offset:         32
        .size:           8
        .value_kind:     global_buffer
      - .address_space:  global
        .offset:         40
        .size:           8
        .value_kind:     global_buffer
      - .actual_access:  read_only
        .address_space:  global
        .offset:         48
        .size:           8
        .value_kind:     global_buffer
      - .actual_access:  read_only
        .address_space:  global
        .offset:         56
        .size:           8
        .value_kind:     global_buffer
      - .address_space:  global
        .offset:         64
        .size:           8
        .value_kind:     global_buffer
      - .address_space:  global
        .offset:         72
        .size:           8
        .value_kind:     global_buffer
      - .actual_access:  read_only
        .address_space:  global
        .offset:         80
        .size:           8
        .value_kind:     global_buffer
      - .actual_access:  read_only
        .address_space:  global
        .offset:         88
        .size:           8
        .value_kind:     global_buffer
      - .offset:         96
        .size:           4
        .value_kind:     hidden_block_count_x
      - .offset:         100
        .size:           4
        .value_kind:     hidden_block_count_y
      - .offset:         104
        .size:           4
        .value_kind:     hidden_block_count_z
      - .offset:         108
        .size:           2
        .value_kind:     hidden_group_size_x
      - .offset:         110
        .size:           2
        .value_kind:     hidden_group_size_y
      - .offset:         112
        .size:           2
        .value_kind:     hidden_group_size_z
      - .offset:         114
        .size:           2
        .value_kind:     hidden_remainder_x
      - .offset:         116
        .size:           2
        .value_kind:     hidden_remainder_y
      - .offset:         118
        .size:           2
        .value_kind:     hidden_remainder_z
      - .offset:         136
        .size:           8
        .value_kind:     hidden_global_offset_x
      - .offset:         144
        .size:           8
        .value_kind:     hidden_global_offset_y
      - .offset:         152
        .size:           8
        .value_kind:     hidden_global_offset_z
      - .offset:         160
        .size:           2
        .value_kind:     hidden_grid_dims
    .group_segment_fixed_size: 26384
    .kernarg_segment_align: 8
    .kernarg_segment_size: 352
    .language:       OpenCL C
    .language_version:
      - 2
      - 0
    .max_flat_workgroup_size: 512
    .name:           _Z12layer_kernelILb1ELi512ELi64EEvPKDv8_DF16_PKfPS0_PiS6_S6_S2_S4_S5_PfPK15HIP_vector_typeIiLj2EEPKi
    .private_segment_fixed_size: 0
    .sgpr_count:     52
    .sgpr_spill_count: 0
    .symbol:         _Z12layer_kernelILb1ELi512ELi64EEvPKDv8_DF16_PKfPS0_PiS6_S6_S2_S4_S5_PfPK15HIP_vector_typeIiLj2EEPKi.kd
    .uniform_work_group_size: 1
    .uses_dynamic_stack: false
    .vgpr_count:     61
    .vgpr_spill_count: 0
    .wavefront_size: 64
  - .agpr_count:     0
    .args:
      - .actual_access:  read_only
        .address_space:  global
        .offset:         0
        .size:           8
        .value_kind:     global_buffer
      - .actual_access:  read_only
        .address_space:  global
        .offset:         8
        .size:           8
        .value_kind:     global_buffer
      - .actual_access:  read_only
        .address_space:  global
        .offset:         16
        .size:           8
        .value_kind:     global_buffer
      - .actual_access:  read_only
        .address_space:  global
        .offset:         24
        .size:           8
        .value_kind:     global_buffer
      - .actual_access:  read_only
        .address_space:  global
        .offset:         32
        .size:           8
        .value_kind:     global_buffer
      - .actual_access:  read_only
        .address_space:  global
        .offset:         40
        .size:           8
        .value_kind:     global_buffer
      - .actual_access:  read_only
        .address_space:  global
        .offset:         48
        .size:           8
        .value_kind:     global_buffer
      - .actual_access:  read_only
        .address_space:  global
        .offset:         56
        .size:           8
        .value_kind:     global_buffer
      - .address_space:  global
        .offset:         64
        .size:           8
        .value_kind:     global_buffer
      - .address_space:  global
        .offset:         72
        .size:           8
        .value_kind:     global_buffer
      - .actual_access:  read_only
        .address_space:  global
        .offset:         80
        .size:           8
        .value_kind:     global_buffer
      - .actual_access:  read_only
        .address_space:  global
        .offset:         88
        .size:           8
        .value_kind:     global_buffer
      - .offset:         96
        .size:           4
        .value_kind:     hidden_block_count_x
      - .offset:         100
        .size:           4
        .value_kind:     hidden_block_count_y
      - .offset:         104
        .size:           4
        .value_kind:     hidden_block_count_z
      - .offset:         108
        .size:           2
        .value_kind:     hidden_group_size_x
      - .offset:         110
        .size:           2
        .value_kind:     hidden_group_size_y
      - .offset:         112
        .size:           2
        .value_kind:     hidden_group_size_z
      - .offset:         114
        .size:           2
        .value_kind:     hidden_remainder_x
      - .offset:         116
        .size:           2
        .value_kind:     hidden_remainder_y
      - .offset:         118
        .size:           2
        .value_kind:     hidden_remainder_z
      - .offset:         136
        .size:           8
        .value_kind:     hidden_global_offset_x
      - .offset:         144
        .size:           8
        .value_kind:     hidden_global_offset_y
      - .offset:         152
        .size:           8
        .value_kind:     hidden_global_offset_z
      - .offset:         160
        .size:           2
        .value_kind:     hidden_grid_dims
    .group_segment_fixed_size: 12932
    .kernarg_segment_align: 8
    .kernarg_segment_size: 352
    .language:       OpenCL C
    .language_version:
      - 2
      - 0
    .max_flat_workgroup_size: 256
    .name:           _Z12layer_kernelILb0ELi256ELi32EEvPKDv8_DF16_PKfPS0_PiS6_S6_S2_S4_S5_PfPK15HIP_vector_typeIiLj2EEPKi
    .private_segment_fixed_size: 0
    .sgpr_count:     32
    .sgpr_spill_count: 0
    .symbol:         _Z12layer_kernelILb0ELi256ELi32EEvPKDv8_DF16_PKfPS0_PiS6_S6_S2_S4_S5_PfPK15HIP_vector_typeIiLj2EEPKi.kd
    .uniform_work_group_size: 1
    .uses_dynamic_stack: false
    .vgpr_count:     64
    .vgpr_spill_count: 0
    .wavefront_size: 64
